# s15
# speedup vs baseline: 1.0723x; 1.0014x over previous
.LBB1_10:
	s_or_b64 exec, exec, s[0:1]
	v_and_b32_e32 v207, 3, v1
	v_and_b32_e32 v174, 15, v0
	v_lshl_or_b32 v175, v207, 6, s75
	s_and_b32 s0, s76, 0x7ffff800
	v_or3_b32 v194, s0, v175, v174
	s_waitcnt lgkmcnt(2)
	v_lshl_add_u64 v[82:83], v[194:195], 2, s[8:9]
	global_load_dword v213, v[82:83], off
	global_load_dword v211, v[82:83], off offset:64
	global_load_dword v210, v[82:83], off offset:128
	global_load_dword v209, v[82:83], off offset:192
	s_waitcnt lgkmcnt(0)
	s_barrier
	v_ashrrev_i32_e32 v208, 8, v0
	v_lshlrev_b32_e32 v162, 9, v208
	v_and_or_b32 v176, v204, 48, v162
	ds_read_b128 v[158:161], v176 offset:34816
	ds_read_b128 v[154:157], v176 offset:34880
	ds_read_b128 v[150:153], v176 offset:34944
	ds_read_b128 v[146:149], v176 offset:35008
	ds_read_b128 v[130:133], v176 offset:35072
	ds_read_b128 v[94:97], v176 offset:35136
	ds_read_b128 v[90:93], v176 offset:35200
	ds_read_b128 v[82:85], v176 offset:35264
	v_mad_i32_i24 v164, v208, s83, v162
	ds_read_b64 v[162:163], v164 offset:35840
	s_cmp_eq_u32 s2, 0x1800000
	s_cselect_b64 s[72:73], -1, 0
	s_cmp_lg_u32 s2, 0x1800000
	s_cselect_b64 s[70:71], -1, 0
	v_mov_b32_e32 v202, 0
	s_and_b64 vcc, exec, s[72:73]
	v_mov_b32_e32 v203, 0
	s_cbranch_vccnz .LBB1_12
	s_add_u32 s0, s22, 0x800000
	v_lshlrev_b32_e32 v166, 7, v0
	s_addc_u32 s1, s90, 0
	v_lshlrev_b32_e32 v165, 11, v0
	v_and_b32_e32 v166, 0x80, v166
	s_movk_i32 s64, 0xf000
	v_and_or_b32 v165, v165, s64, v166
	s_add_u32 s80, s22, 0x800100
	global_load_dword v202, v165, s[0:1]
	s_addc_u32 s81, s90, 0
	global_load_dword v203, v165, s[80:81]
